# expert GEMM1 (both layers): first K-tile of every unit peeled with C = 0 in its 32 MFMAs, the 128 accumulator-zeroing moves per unit removed
# baseline (speedup 1.0000x reference)
; template <class Epi, class Sched, bool GATHER, bool FP8 = false>
; __device__ __forceinline__ void gemm_phase(LAS unsigned char* lds, LAS int* idx, const Gemm g, const Sched& S, const Epi& E) {
;     ...
;     f32x4 acc[2][2][4][2];
; #pragma unroll
;     for (int a = 0; a < 2; ++a)
; #pragma unroll
;         for (int b = 0; b < 2; ++b)
; #pragma unroll
;             for (int m = 0; m < 4; ++m)
; #pragma unroll
;                 for (int n = 0; n < 2; ++n) acc[a][b][m][n] = (f32x4){0.f, 0.f, 0.f, 0.f};
;     bf16x8 At[4][2], B0[2][2], B1[2][2]; i32x8 At8[4], B08[2], B18[2];
;     const unsigned epi_scale = 0x01010101u * (unsigned)(127 + Epi::SEXP);
;     const unsigned one_scale = 0x7f7f7f7fu;
;     const char* cA = (const char*)g.A + (GATHER ? (size_t)0 : (size_t)cur.pm * tstep + (size_t)cur.be * g.astride);
;     const char* cB = (const char*)g.Bt + (size_t)cur.be * g.bstride + (size_t)cur.pn * tstep;
;     unsigned gc[2][2] = {{0u, 0u}, {0u, 0u}};
.LBB0_757:
	s_xor_b64 s[34:35], s[34:35], -1
	s_cmp_lg_u32 s29, 0
	s_cselect_b64 s[36:37], -1, 0
	v_lshl_add_u32 v2, s25, 2, v1
	s_add_u32 s25, s38, 0x100
	s_mov_b32 s23, 0
	v_lshl_add_u32 v250, v195, 2, v2
	v_lshl_add_u32 v251, v232, 2, v2
	s_addc_u32 s29, s39, 0
	s_mov_b64 s[42:43], 0

; #define PG8_STAGE(bufoff, gbase, voff) do { _Pragma("unroll") for (int _i = 0; _i < 2; ++_i) \
;         __builtin_amdgcn_global_load_lds((const unsigned*)((const char*)(gbase) + (voff)[_i]), (LAS unsigned*)(lds + (bufoff) + ldsw + _i * 8192), 16, 0, 0); } while (0)
; #define PG8_STAGEA(bufoff, h, ap, kb, go) do { if constexpr (GATHER) { PG8_STAGE(bufoff, (const char*)g.A + (kb), go[h]); } else { PG8_STAGE(bufoff, (ap) + (h) * hstep, voffA); } } while (0)
; #define PG8_WAIT_L(n) asm volatile("s_waitcnt lgkmcnt(" #n ")" ::: "memory")
; #define PG8_WAIT_V8R() do { if (relax) { if (GATHER && wid == 0 && has_next) asm volatile("s_waitcnt vmcnt(%0)" :: "n"(9 + Epi::NSTORES) : "memory"); else asm volatile("s_waitcnt vmcnt(%0)" :: "n"(8 + Epi::NSTORES) : "memory"); } else PG8_WAIT_V(8); } while (0)
; #define PG8_BAR __builtin_amdgcn_s_barrier()
; template <class Epi, class Sched, bool GATHER, bool FP8 = false>
; __device__ __forceinline__ void gemm_phase(LAS unsigned char* lds, LAS int* idx, const Gemm g, const Sched& S, const Epi& E) {
;     ...
;             const bool last = (t == nt - 2);
;             const char* a1 = cA + (size_t)(t + 1) * kstep;
;             const char* a2 = last ? nA : cA + (size_t)(t + 2) * kstep; const char* b2 = last ? nB : cB + (size_t)(t + 2) * kstep;
;             const char* a3 = a2 + kstep; const char* b3 = b2 + kstep;
;             const size_t k1 = (size_t)(t + 1) * kstep, k2 = last ? (size_t)0 : (size_t)(t + 2) * kstep, k3 = k2 + kstep;
;             unsigned g2[2][2];
; #pragma unroll
;             for (int h = 0; h < 2; ++h)
; #pragma unroll
;                 for (int i = 0; i < 2; ++i) g2[h][i] = gc[h][i];
;             if constexpr (GATHER) { if (last && has_next) PG8_GIDX(g2, ((ui + 1) & 1) * BM); }
;             const int relax = __builtin_amdgcn_readfirstlane(((t == 0) && (ui > 0)) ? 1 : 0);
;             PG8_LDB(B0, 0, 0); PG8_LDB(B1, 0, 1); PG8_SCHED; PG8_LDA(At, 0, 0); PG8_STAGEA(PG8_SA(1, 1), 1, a1, k1, gc);
;             PG8_WAIT_V8R(); PG8_WAIT_L(0); PG8_BAR; PG8_MMA(0, 0, At, B0); PG8_MMA(0, 1, At, B1); PG8_BAR; PG8_SCHED;
;             PG8_LDA(At, 0, 1); PG8_STAGE(PG8_SB(0, 0), b2, voffB); PG8_STAGE(PG8_SB(0, 1), b2 + hstepB, voffB); PG8_STAGEA(PG8_SA(0, 0), 0, a2, k2, g2);
;             PG8_WAIT_V8R(); PG8_WAIT_L(0); PG8_BAR; PG8_MMA(1, 0, At, B0); PG8_MMA(1, 1, At, B1); PG8_BAR; PG8_SCHED;
.Lpl758_767:
	s_add_u32 s40, s42, 0x100
	s_addc_u32 s41, s43, 0
	s_add_u32 s46, s25, s42
	s_addc_u32 s47, s29, s43
	s_waitcnt lgkmcnt(0)
	s_and_b64 s[42:43], s[38:39], exec
	s_cselect_b32 s43, s27, s47
	s_cselect_b32 s42, s26, s46
	s_cselect_b32 s46, 0, s41
	s_cselect_b32 s47, 0, s40
	s_barrier
	s_setprio 1
	s_waitcnt lgkmcnt(0)
	v_mfma_scale_f32_16x16x128_f8f6f4 v[190:193], v[26:33], v[58:65], 0, v247, v247 op_sel_hi:[0,0,0]
	v_mfma_scale_f32_16x16x128_f8f6f4 v[186:189], v[18:25], v[58:65], 0, v247, v247 op_sel_hi:[0,0,0]
	v_mfma_scale_f32_16x16x128_f8f6f4 v[174:177], v[26:33], v[50:57], 0, v247, v247 op_sel_hi:[0,0,0]
	v_mfma_scale_f32_16x16x128_f8f6f4 v[170:173], v[18:25], v[50:57], 0, v247, v247 op_sel_hi:[0,0,0]
	v_mfma_scale_f32_16x16x128_f8f6f4 v[158:161], v[26:33], v[42:49], 0, v247, v247 op_sel_hi:[0,0,0]
	v_mfma_scale_f32_16x16x128_f8f6f4 v[154:157], v[18:25], v[42:49], 0, v247, v247 op_sel_hi:[0,0,0]
	v_mfma_scale_f32_16x16x128_f8f6f4 v[142:145], v[26:33], v[34:41], 0, v247, v247 op_sel_hi:[0,0,0]
	v_mfma_scale_f32_16x16x128_f8f6f4 v[138:141], v[18:25], v[34:41], 0, v247, v247 op_sel_hi:[0,0,0]
	s_setprio 0
	s_setprio 1
	v_mfma_scale_f32_16x16x128_f8f6f4 v[182:185], v[10:17], v[58:65], 0, v247, v247 op_sel_hi:[0,0,0]
	v_mfma_scale_f32_16x16x128_f8f6f4 v[178:181], v[2:9], v[58:65], 0, v247, v247 op_sel_hi:[0,0,0]
	v_mfma_scale_f32_16x16x128_f8f6f4 v[166:169], v[10:17], v[50:57], 0, v247, v247 op_sel_hi:[0,0,0]
	v_mfma_scale_f32_16x16x128_f8f6f4 v[162:165], v[2:9], v[50:57], 0, v247, v247 op_sel_hi:[0,0,0]
	v_mfma_scale_f32_16x16x128_f8f6f4 v[150:153], v[10:17], v[42:49], 0, v247, v247 op_sel_hi:[0,0,0]
	v_mfma_scale_f32_16x16x128_f8f6f4 v[146:149], v[2:9], v[42:49], 0, v247, v247 op_sel_hi:[0,0,0]
	v_mfma_scale_f32_16x16x128_f8f6f4 v[134:137], v[10:17], v[34:41], 0, v247, v247 op_sel_hi:[0,0,0]
	v_mfma_scale_f32_16x16x128_f8f6f4 v[130:133], v[2:9], v[34:41], 0, v247, v247 op_sel_hi:[0,0,0]
	s_setprio 0
	s_barrier
	s_mov_b32 m0, s55
	v_lshl_add_u64 v[218:219], s[42:43], 0, v[196:197]
	v_lshl_add_u64 v[220:221], s[42:43], 0, v[198:199]
	s_add_u32 s42, s42, s8
	ds_read_b128 v[58:61], v248 offset:16384
	ds_read_b128 v[62:65], v248 offset:17408
	ds_read_b128 v[50:53], v248 offset:18432
	ds_read_b128 v[54:57], v248 offset:19456
	ds_read_b128 v[42:45], v248 offset:20480
	ds_read_b128 v[46:49], v248 offset:21504
	ds_read_b128 v[34:37], v248 offset:22528
	ds_read_b128 v[38:41], v248 offset:23552
	global_load_lds_dwordx4 v[218:219], off
	s_mov_b32 m0, s56
	s_addc_u32 s43, s43, s9
	global_load_lds_dwordx4 v[220:221], off
	v_lshl_add_u64 v[222:223], s[42:43], 0, v[196:197]
	s_mov_b32 m0, s57
	v_lshl_add_u64 v[224:225], s[42:43], 0, v[198:199]
	global_load_lds_dwordx4 v[222:223], off
	s_mov_b32 m0, s58
	s_add_u32 s42, s6, s47
	global_load_lds_dwordx4 v[224:225], off
	s_addc_u32 s43, s7, s46
	s_mov_b32 m0, s54
	s_mov_b64 s[46:47], -1
	global_load_lds_dwordx4 v208, s[42:43]
	s_mov_b32 m0, s59
	s_and_b64 vcc, exec, s[44:45]
	global_load_lds_dwordx4 v216, s[42:43]
	s_cbranch_vccz .Lpl758_769
	s_waitcnt vmcnt(8)
	s_mov_b64 s[46:47], 0

; #define PG8_WAIT_L(n) asm volatile("s_waitcnt lgkmcnt(" #n ")" ::: "memory")
; #define PG8_WAIT_V8R() do { if (relax) { if (GATHER && wid == 0 && has_next) asm volatile("s_waitcnt vmcnt(%0)" :: "n"(9 + Epi::NSTORES) : "memory"); else asm volatile("s_waitcnt vmcnt(%0)" :: "n"(8 + Epi::NSTORES) : "memory"); } else PG8_WAIT_V(8); } while (0)
; #define PG8_BAR __builtin_amdgcn_s_barrier()
; #define PG8_SCHED __builtin_amdgcn_sched_barrier(0)
; template <class Epi, class Sched, bool GATHER, bool FP8 = false>
; __device__ __forceinline__ void gemm_phase(LAS unsigned char* lds, LAS int* idx, const Gemm g, const Sched& S, const Epi& E) {
;     ...
;             PG8_WAIT_V8R(); PG8_WAIT_L(0); PG8_BAR; PG8_MMA(1, 0, At, B0); PG8_MMA(1, 1, At, B1); PG8_BAR; PG8_SCHED;
.Lpl758_774:
	s_waitcnt lgkmcnt(0)
	v_mov_b32_e32 v217, v209
	v_lshl_add_u64 v[226:227], s[42:43], 0, v[208:209]
	v_lshl_add_u64 v[228:229], s[42:43], 0, v[216:217]
	s_barrier
	s_setprio 1
	s_waitcnt lgkmcnt(0)
	v_mfma_scale_f32_16x16x128_f8f6f4 v[126:129], v[26:33], v[58:65], 0, v247, v247 op_sel_hi:[0,0,0]
	v_mfma_scale_f32_16x16x128_f8f6f4 v[122:125], v[18:25], v[58:65], 0, v247, v247 op_sel_hi:[0,0,0]
	v_mfma_scale_f32_16x16x128_f8f6f4 v[110:113], v[26:33], v[50:57], 0, v247, v247 op_sel_hi:[0,0,0]
	v_mfma_scale_f32_16x16x128_f8f6f4 v[106:109], v[18:25], v[50:57], 0, v247, v247 op_sel_hi:[0,0,0]
	v_mfma_scale_f32_16x16x128_f8f6f4 v[94:97], v[26:33], v[42:49], 0, v247, v247 op_sel_hi:[0,0,0]
	v_mfma_scale_f32_16x16x128_f8f6f4 v[90:93], v[18:25], v[42:49], 0, v247, v247 op_sel_hi:[0,0,0]
	v_mfma_scale_f32_16x16x128_f8f6f4 v[78:81], v[26:33], v[34:41], 0, v247, v247 op_sel_hi:[0,0,0]
	v_mfma_scale_f32_16x16x128_f8f6f4 v[74:77], v[18:25], v[34:41], 0, v247, v247 op_sel_hi:[0,0,0]
	s_setprio 0
	s_setprio 1
	v_mfma_scale_f32_16x16x128_f8f6f4 v[118:121], v[10:17], v[58:65], 0, v247, v247 op_sel_hi:[0,0,0]
	v_mfma_scale_f32_16x16x128_f8f6f4 v[114:117], v[2:9], v[58:65], 0, v247, v247 op_sel_hi:[0,0,0]
	v_mfma_scale_f32_16x16x128_f8f6f4 v[102:105], v[10:17], v[50:57], 0, v247, v247 op_sel_hi:[0,0,0]
	v_mfma_scale_f32_16x16x128_f8f6f4 v[98:101], v[2:9], v[50:57], 0, v247, v247 op_sel_hi:[0,0,0]
	v_mfma_scale_f32_16x16x128_f8f6f4 v[86:89], v[10:17], v[42:49], 0, v247, v247 op_sel_hi:[0,0,0]
	v_mfma_scale_f32_16x16x128_f8f6f4 v[82:85], v[2:9], v[42:49], 0, v247, v247 op_sel_hi:[0,0,0]
	v_mfma_scale_f32_16x16x128_f8f6f4 v[70:73], v[10:17], v[34:41], 0, v247, v247 op_sel_hi:[0,0,0]
	v_mfma_scale_f32_16x16x128_f8f6f4 v[66:69], v[2:9], v[34:41], 0, v247, v247 op_sel_hi:[0,0,0]
	s_branch .Lpl758_join

; #define PG8_STAGE(bufoff, gbase, voff) do { _Pragma("unroll") for (int _i = 0; _i < 2; ++_i) \
;         __builtin_amdgcn_global_load_lds((const unsigned*)((const char*)(gbase) + (voff)[_i]), (LAS unsigned*)(lds + (bufoff) + ldsw + _i * 8192), 16, 0, 0); } while (0)
; #define PG8_STAGEA(bufoff, h, ap, kb, go) do { if constexpr (GATHER) { PG8_STAGE(bufoff, (const char*)g.A + (kb), go[h]); } else { PG8_STAGE(bufoff, (ap) + (h) * hstep, voffA); } } while (0)
; #define PG8_WAIT_V(n) asm volatile("s_waitcnt vmcnt(" #n ")" ::: "memory")
; #define PG8_WAIT_L(n) asm volatile("s_waitcnt lgkmcnt(" #n ")" ::: "memory")
; #define PG8_BAR __builtin_amdgcn_s_barrier()
; #define PG8_SCHED __builtin_amdgcn_sched_barrier(0)
; template <class Epi, class Sched, bool GATHER, bool FP8 = false>
; __device__ __forceinline__ void gemm_phase(LAS unsigned char* lds, LAS int* idx, const Gemm g, const Sched& S, const Epi& E) {
;     ...
;             PG8_LDB(B0, 1, 0); PG8_LDB(B1, 1, 1); PG8_SCHED; PG8_LDA(At, 1, 0); PG8_STAGEA(PG8_SA(0, 1), 1, a2, k2, g2);
;             PG8_WAIT_V(8); PG8_WAIT_L(0); PG8_BAR; PG8_MMA(0, 0, At, B0); PG8_MMA(0, 1, At, B1); PG8_BAR; PG8_SCHED;
;             PG8_LDA(At, 1, 1); PG8_STAGE(PG8_SB(1, 0), b3, voffB); PG8_STAGE(PG8_SB(1, 1), b3 + hstepB, voffB); PG8_STAGEA(PG8_SA(1, 0), 0, a3, k3, g2);
;             PG8_WAIT_V(8); PG8_WAIT_L(0); PG8_BAR; PG8_MMA(1, 0, At, B0); PG8_MMA(1, 1, At, B1); PG8_BAR; PG8_SCHED;
;             if constexpr (GATHER) { if (last) { _Pragma("unroll") for (int h = 0; h < 2; ++h) _Pragma("unroll") for (int i = 0; i < 2; ++i) gc[h][i] = g2[h][i]; } }
.Lpl758_join:
	s_setprio 0
	s_barrier
	ds_read_b128 v[2:5], v238
	ds_read_b128 v[6:9], v239
	ds_read_b128 v[10:13], v240
	ds_read_b128 v[14:17], v241
	ds_read_b128 v[18:21], v242
	ds_read_b128 v[22:25], v243
	ds_read_b128 v[26:29], v244
	ds_read_b128 v[30:33], v245
	s_mov_b32 m0, s60
	ds_read_b128 v[34:37], v248 offset:32768
	ds_read_b128 v[38:41], v248 offset:33792
	ds_read_b128 v[42:45], v248 offset:34816
	ds_read_b128 v[46:49], v248 offset:35840
	ds_read_b128 v[50:53], v248 offset:36864
	ds_read_b128 v[54:57], v248 offset:37888
	ds_read_b128 v[58:61], v248 offset:38912
	ds_read_b128 v[62:65], v248 offset:39936
	global_load_lds_dwordx4 v212, s[42:43]
	s_mov_b32 m0, s61
	s_nop 0
	global_load_lds_dwordx4 v214, s[42:43]
	s_waitcnt vmcnt(8)
	s_waitcnt lgkmcnt(0)
	s_barrier
	s_setprio 1
	s_waitcnt lgkmcnt(0)
	v_mfma_scale_f32_16x16x128_f8f6f4 v[190:193], v[2:9], v[34:41], v[190:193], v247, v247 op_sel_hi:[0,0,0]
	v_mfma_scale_f32_16x16x128_f8f6f4 v[186:189], v[10:17], v[34:41], v[186:189], v247, v247 op_sel_hi:[0,0,0]
	v_mfma_scale_f32_16x16x128_f8f6f4 v[174:177], v[2:9], v[42:49], v[174:177], v247, v247 op_sel_hi:[0,0,0]
	v_mfma_scale_f32_16x16x128_f8f6f4 v[170:173], v[10:17], v[42:49], v[170:173], v247, v247 op_sel_hi:[0,0,0]
	v_mfma_scale_f32_16x16x128_f8f6f4 v[158:161], v[2:9], v[50:57], v[158:161], v247, v247 op_sel_hi:[0,0,0]
	v_mfma_scale_f32_16x16x128_f8f6f4 v[154:157], v[10:17], v[50:57], v[154:157], v247, v247 op_sel_hi:[0,0,0]
	v_mfma_scale_f32_16x16x128_f8f6f4 v[142:145], v[2:9], v[58:65], v[142:145], v247, v247 op_sel_hi:[0,0,0]
	v_mfma_scale_f32_16x16x128_f8f6f4 v[138:141], v[10:17], v[58:65], v[138:141], v247, v247 op_sel_hi:[0,0,0]
	s_setprio 0
	s_setprio 1
	v_mfma_scale_f32_16x16x128_f8f6f4 v[182:185], v[18:25], v[34:41], v[182:185], v247, v247 op_sel_hi:[0,0,0]
	v_mfma_scale_f32_16x16x128_f8f6f4 v[178:181], v[26:33], v[34:41], v[178:181], v247, v247 op_sel_hi:[0,0,0]
	v_mfma_scale_f32_16x16x128_f8f6f4 v[166:169], v[18:25], v[42:49], v[166:169], v247, v247 op_sel_hi:[0,0,0]
	v_mfma_scale_f32_16x16x128_f8f6f4 v[162:165], v[26:33], v[42:49], v[162:165], v247, v247 op_sel_hi:[0,0,0]
	v_mfma_scale_f32_16x16x128_f8f6f4 v[150:153], v[18:25], v[50:57], v[150:153], v247, v247 op_sel_hi:[0,0,0]
	v_mfma_scale_f32_16x16x128_f8f6f4 v[146:149], v[26:33], v[50:57], v[146:149], v247, v247 op_sel_hi:[0,0,0]
	v_mfma_scale_f32_16x16x128_f8f6f4 v[134:137], v[18:25], v[58:65], v[134:137], v247, v247 op_sel_hi:[0,0,0]
	v_mfma_scale_f32_16x16x128_f8f6f4 v[130:133], v[26:33], v[58:65], v[130:133], v247, v247 op_sel_hi:[0,0,0]
	s_setprio 0
	s_barrier
	s_mov_b32 m0, s64
	v_lshl_add_u64 v[218:219], v[218:219], 0, s[12:13]
	ds_read_b128 v[34:37], v248 offset:49152
	ds_read_b128 v[38:41], v248 offset:50176
	ds_read_b128 v[42:45], v248 offset:51200
	ds_read_b128 v[46:49], v248 offset:52224
	ds_read_b128 v[50:53], v248 offset:53248
	ds_read_b128 v[54:57], v248 offset:54272
	ds_read_b128 v[58:61], v248 offset:55296
	ds_read_b128 v[62:65], v248 offset:56320
	global_load_lds_dwordx4 v[218:219], off
	v_lshl_add_u64 v[218:219], v[220:221], 0, s[12:13]
	s_mov_b32 m0, s65
	s_nop 0
	global_load_lds_dwordx4 v[218:219], off
	v_lshl_add_u64 v[218:219], v[222:223], 0, s[12:13]
	s_mov_b32 m0, s71
	s_nop 0
	global_load_lds_dwordx4 v[218:219], off
	v_lshl_add_u64 v[218:219], v[224:225], 0, s[12:13]
	s_mov_b32 m0, s72
	s_nop 0
	global_load_lds_dwordx4 v[218:219], off
	v_lshl_add_u64 v[218:219], v[226:227], 0, s[12:13]
	s_mov_b32 m0, s66
	s_nop 0
	global_load_lds_dwordx4 v[218:219], off
	v_lshl_add_u64 v[218:219], v[228:229], 0, s[12:13]
	s_mov_b32 m0, s67
	s_nop 0
	global_load_lds_dwordx4 v[218:219], off
	s_waitcnt vmcnt(8)
	s_waitcnt lgkmcnt(0)
	s_barrier
	s_setprio 1
	s_waitcnt lgkmcnt(0)
	v_mfma_scale_f32_16x16x128_f8f6f4 v[126:129], v[2:9], v[34:41], v[126:129], v247, v247 op_sel_hi:[0,0,0]
	v_mfma_scale_f32_16x16x128_f8f6f4 v[122:125], v[10:17], v[34:41], v[122:125], v247, v247 op_sel_hi:[0,0,0]
	v_mfma_scale_f32_16x16x128_f8f6f4 v[110:113], v[2:9], v[42:49], v[110:113], v247, v247 op_sel_hi:[0,0,0]
	v_mfma_scale_f32_16x16x128_f8f6f4 v[106:109], v[10:17], v[42:49], v[106:109], v247, v247 op_sel_hi:[0,0,0]
	v_mfma_scale_f32_16x16x128_f8f6f4 v[94:97], v[2:9], v[50:57], v[94:97], v247, v247 op_sel_hi:[0,0,0]
	v_mfma_scale_f32_16x16x128_f8f6f4 v[90:93], v[10:17], v[50:57], v[90:93], v247, v247 op_sel_hi:[0,0,0]
	v_mfma_scale_f32_16x16x128_f8f6f4 v[78:81], v[2:9], v[58:65], v[78:81], v247, v247 op_sel_hi:[0,0,0]
	v_mfma_scale_f32_16x16x128_f8f6f4 v[74:77], v[10:17], v[58:65], v[74:77], v247, v247 op_sel_hi:[0,0,0]
	s_setprio 0
	s_setprio 1
	v_mfma_scale_f32_16x16x128_f8f6f4 v[118:121], v[18:25], v[34:41], v[118:121], v247, v247 op_sel_hi:[0,0,0]
	v_mfma_scale_f32_16x16x128_f8f6f4 v[114:117], v[26:33], v[34:41], v[114:117], v247, v247 op_sel_hi:[0,0,0]
	v_mfma_scale_f32_16x16x128_f8f6f4 v[102:105], v[18:25], v[42:49], v[102:105], v247, v247 op_sel_hi:[0,0,0]
	v_mfma_scale_f32_16x16x128_f8f6f4 v[98:101], v[26:33], v[42:49], v[98:101], v247, v247 op_sel_hi:[0,0,0]
	v_mfma_scale_f32_16x16x128_f8f6f4 v[86:89], v[18:25], v[50:57], v[86:89], v247, v247 op_sel_hi:[0,0,0]
	v_mfma_scale_f32_16x16x128_f8f6f4 v[82:85], v[26:33], v[50:57], v[82:85], v247, v247 op_sel_hi:[0,0,0]
	v_mfma_scale_f32_16x16x128_f8f6f4 v[70:73], v[18:25], v[58:65], v[70:73], v247, v247 op_sel_hi:[0,0,0]
	v_mfma_scale_f32_16x16x128_f8f6f4 v[66:69], v[26:33], v[58:65], v[66:69], v247, v247 op_sel_hi:[0,0,0]
	s_setprio 0
	s_barrier
	s_andn2_b64 vcc, exec, s[38:39]
	s_cbranch_vccnz .LBB0_776
	v_mov_b32_e32 v200, v208
	v_mov_b32_e32 v204, v216
	v_mov_b32_e32 v202, v212
	v_mov_b32_e32 v206, v214

; template <class Epi, class Sched, bool GATHER, bool FP8 = false>
; __device__ __forceinline__ void gemm_phase(LAS unsigned char* lds, LAS int* idx, const Gemm g, const Sched& S, const Epi& E) {
;     ...
;     f32x4 acc[2][2][4][2];
; #pragma unroll
;     for (int a = 0; a < 2; ++a)
; #pragma unroll
;         for (int b = 0; b < 2; ++b)
; #pragma unroll
;             for (int m = 0; m < 4; ++m)
; #pragma unroll
;                 for (int n = 0; n < 2; ++n) acc[a][b][m][n] = (f32x4){0.f, 0.f, 0.f, 0.f};
;     bf16x8 At[4][2], B0[2][2], B1[2][2]; i32x8 At8[4], B08[2], B18[2];
;     const unsigned epi_scale = 0x01010101u * (unsigned)(127 + Epi::SEXP);
;     const unsigned one_scale = 0x7f7f7f7fu;
;     const char* cA = (const char*)g.A + (GATHER ? (size_t)0 : (size_t)cur.pm * tstep + (size_t)cur.be * g.astride);
;     const char* cB = (const char*)g.Bt + (size_t)cur.be * g.bstride + (size_t)cur.pn * tstep;
;     unsigned gc[2][2] = {{0u, 0u}, {0u, 0u}};
.LBB0_1530:
	s_xor_b64 s[34:35], s[34:35], -1
	s_cmp_lg_u32 s40, 0
	s_cselect_b64 s[36:37], -1, 0
	v_lshl_add_u32 v2, s25, 2, v1
	s_add_u32 s25, s38, 0x100
	s_mov_b32 s23, 0
	v_lshl_add_u32 v249, v195, 2, v2
	v_lshl_add_u32 v250, v231, 2, v2
	s_addc_u32 s80, s39, 0
	s_mov_b64 s[42:43], 0

; #define PG8_STAGE(bufoff, gbase, voff) do { _Pragma("unroll") for (int _i = 0; _i < 2; ++_i) \
;         __builtin_amdgcn_global_load_lds((const unsigned*)((const char*)(gbase) + (voff)[_i]), (LAS unsigned*)(lds + (bufoff) + ldsw + _i * 8192), 16, 0, 0); } while (0)
; #define PG8_STAGEA(bufoff, h, ap, kb, go) do { if constexpr (GATHER) { PG8_STAGE(bufoff, (const char*)g.A + (kb), go[h]); } else { PG8_STAGE(bufoff, (ap) + (h) * hstep, voffA); } } while (0)
; #define PG8_WAIT_L(n) asm volatile("s_waitcnt lgkmcnt(" #n ")" ::: "memory")
; #define PG8_WAIT_V8R() do { if (relax) { if (GATHER && wid == 0 && has_next) asm volatile("s_waitcnt vmcnt(%0)" :: "n"(9 + Epi::NSTORES) : "memory"); else asm volatile("s_waitcnt vmcnt(%0)" :: "n"(8 + Epi::NSTORES) : "memory"); } else PG8_WAIT_V(8); } while (0)
; #define PG8_BAR __builtin_amdgcn_s_barrier()
; template <class Epi, class Sched, bool GATHER, bool FP8 = false>
; __device__ __forceinline__ void gemm_phase(LAS unsigned char* lds, LAS int* idx, const Gemm g, const Sched& S, const Epi& E) {
;     ...
;             const bool last = (t == nt - 2);
;             const char* a1 = cA + (size_t)(t + 1) * kstep;
;             const char* a2 = last ? nA : cA + (size_t)(t + 2) * kstep; const char* b2 = last ? nB : cB + (size_t)(t + 2) * kstep;
;             const char* a3 = a2 + kstep; const char* b3 = b2 + kstep;
;             const size_t k1 = (size_t)(t + 1) * kstep, k2 = last ? (size_t)0 : (size_t)(t + 2) * kstep, k3 = k2 + kstep;
;             unsigned g2[2][2];
; #pragma unroll
;             for (int h = 0; h < 2; ++h)
; #pragma unroll
;                 for (int i = 0; i < 2; ++i) g2[h][i] = gc[h][i];
;             if constexpr (GATHER) { if (last && has_next) PG8_GIDX(g2, ((ui + 1) & 1) * BM); }
;             const int relax = __builtin_amdgcn_readfirstlane(((t == 0) && (ui > 0)) ? 1 : 0);
;             PG8_LDB(B0, 0, 0); PG8_LDB(B1, 0, 1); PG8_SCHED; PG8_LDA(At, 0, 0); PG8_STAGEA(PG8_SA(1, 1), 1, a1, k1, gc);
;             PG8_WAIT_V8R(); PG8_WAIT_L(0); PG8_BAR; PG8_MMA(0, 0, At, B0); PG8_MMA(0, 1, At, B1); PG8_BAR; PG8_SCHED;
;             PG8_LDA(At, 0, 1); PG8_STAGE(PG8_SB(0, 0), b2, voffB); PG8_STAGE(PG8_SB(0, 1), b2 + hstepB, voffB); PG8_STAGEA(PG8_SA(0, 0), 0, a2, k2, g2);
;             PG8_WAIT_V8R(); PG8_WAIT_L(0); PG8_BAR; PG8_MMA(1, 0, At, B0); PG8_MMA(1, 1, At, B1); PG8_BAR; PG8_SCHED;
.Lpl1531_1540:
	s_add_u32 s40, s42, 0x100
	s_addc_u32 s41, s43, 0
	s_add_u32 s46, s25, s42
	s_addc_u32 s47, s80, s43
	s_waitcnt lgkmcnt(0)
	s_and_b64 s[42:43], s[38:39], exec
	s_cselect_b32 s43, s27, s47
	s_cselect_b32 s42, s26, s46
	s_cselect_b32 s46, 0, s41
	s_cselect_b32 s47, 0, s40
	s_barrier
	s_setprio 1
	s_waitcnt lgkmcnt(0)
	v_mfma_scale_f32_16x16x128_f8f6f4 v[190:193], v[26:33], v[58:65], 0, v246, v246 op_sel_hi:[0,0,0]
	v_mfma_scale_f32_16x16x128_f8f6f4 v[186:189], v[18:25], v[58:65], 0, v246, v246 op_sel_hi:[0,0,0]
	v_mfma_scale_f32_16x16x128_f8f6f4 v[174:177], v[26:33], v[50:57], 0, v246, v246 op_sel_hi:[0,0,0]
	v_mfma_scale_f32_16x16x128_f8f6f4 v[170:173], v[18:25], v[50:57], 0, v246, v246 op_sel_hi:[0,0,0]
	v_mfma_scale_f32_16x16x128_f8f6f4 v[158:161], v[26:33], v[42:49], 0, v246, v246 op_sel_hi:[0,0,0]
	v_mfma_scale_f32_16x16x128_f8f6f4 v[154:157], v[18:25], v[42:49], 0, v246, v246 op_sel_hi:[0,0,0]
	v_mfma_scale_f32_16x16x128_f8f6f4 v[142:145], v[26:33], v[34:41], 0, v246, v246 op_sel_hi:[0,0,0]
	v_mfma_scale_f32_16x16x128_f8f6f4 v[138:141], v[18:25], v[34:41], 0, v246, v246 op_sel_hi:[0,0,0]
	s_setprio 0
	s_setprio 1
	v_mfma_scale_f32_16x16x128_f8f6f4 v[182:185], v[10:17], v[58:65], 0, v246, v246 op_sel_hi:[0,0,0]
	v_mfma_scale_f32_16x16x128_f8f6f4 v[178:181], v[2:9], v[58:65], 0, v246, v246 op_sel_hi:[0,0,0]
	v_mfma_scale_f32_16x16x128_f8f6f4 v[166:169], v[10:17], v[50:57], 0, v246, v246 op_sel_hi:[0,0,0]
	v_mfma_scale_f32_16x16x128_f8f6f4 v[162:165], v[2:9], v[50:57], 0, v246, v246 op_sel_hi:[0,0,0]
	v_mfma_scale_f32_16x16x128_f8f6f4 v[150:153], v[10:17], v[42:49], 0, v246, v246 op_sel_hi:[0,0,0]
	v_mfma_scale_f32_16x16x128_f8f6f4 v[146:149], v[2:9], v[42:49], 0, v246, v246 op_sel_hi:[0,0,0]
	v_mfma_scale_f32_16x16x128_f8f6f4 v[134:137], v[10:17], v[34:41], 0, v246, v246 op_sel_hi:[0,0,0]
	v_mfma_scale_f32_16x16x128_f8f6f4 v[130:133], v[2:9], v[34:41], 0, v246, v246 op_sel_hi:[0,0,0]
	s_setprio 0
	s_barrier
	s_mov_b32 m0, s54
	v_lshl_add_u64 v[218:219], s[42:43], 0, v[196:197]
	v_lshl_add_u64 v[220:221], s[42:43], 0, v[198:199]
	s_add_u32 s42, s42, s8
	ds_read_b128 v[58:61], v247 offset:16384
	ds_read_b128 v[62:65], v247 offset:17408
	ds_read_b128 v[50:53], v247 offset:18432
	ds_read_b128 v[54:57], v247 offset:19456
	ds_read_b128 v[42:45], v247 offset:20480
	ds_read_b128 v[46:49], v247 offset:21504
	ds_read_b128 v[34:37], v247 offset:22528
	ds_read_b128 v[38:41], v247 offset:23552
	global_load_lds_dwordx4 v[218:219], off
	s_mov_b32 m0, s55
	s_addc_u32 s43, s43, s9
	global_load_lds_dwordx4 v[220:221], off
	v_lshl_add_u64 v[222:223], s[42:43], 0, v[196:197]
	s_mov_b32 m0, s56
	v_lshl_add_u64 v[224:225], s[42:43], 0, v[198:199]
	global_load_lds_dwordx4 v[222:223], off
	s_mov_b32 m0, s57
	s_add_u32 s42, s6, s47
	global_load_lds_dwordx4 v[224:225], off
	s_addc_u32 s43, s7, s46
	s_mov_b32 m0, s52
	s_mov_b64 s[46:47], -1
	global_load_lds_dwordx4 v208, s[42:43]
	s_mov_b32 m0, s58
	s_and_b64 vcc, exec, s[44:45]
	global_load_lds_dwordx4 v216, s[42:43]
	s_cbranch_vccz .Lpl1531_1542
	s_waitcnt vmcnt(8)
	s_mov_b64 s[46:47], 0

; #define PG8_WAIT_L(n) asm volatile("s_waitcnt lgkmcnt(" #n ")" ::: "memory")
; #define PG8_WAIT_V8R() do { if (relax) { if (GATHER && wid == 0 && has_next) asm volatile("s_waitcnt vmcnt(%0)" :: "n"(9 + Epi::NSTORES) : "memory"); else asm volatile("s_waitcnt vmcnt(%0)" :: "n"(8 + Epi::NSTORES) : "memory"); } else PG8_WAIT_V(8); } while (0)
; #define PG8_BAR __builtin_amdgcn_s_barrier()
; #define PG8_SCHED __builtin_amdgcn_sched_barrier(0)
; template <class Epi, class Sched, bool GATHER, bool FP8 = false>
; __device__ __forceinline__ void gemm_phase(LAS unsigned char* lds, LAS int* idx, const Gemm g, const Sched& S, const Epi& E) {
;     ...
;             PG8_WAIT_V8R(); PG8_WAIT_L(0); PG8_BAR; PG8_MMA(1, 0, At, B0); PG8_MMA(1, 1, At, B1); PG8_BAR; PG8_SCHED;
.Lpl1531_1547:
	s_waitcnt lgkmcnt(0)
	v_mov_b32_e32 v217, v209
	v_lshl_add_u64 v[226:227], s[42:43], 0, v[208:209]
	v_lshl_add_u64 v[228:229], s[42:43], 0, v[216:217]
	s_barrier
	s_setprio 1
	s_waitcnt lgkmcnt(0)
	v_mfma_scale_f32_16x16x128_f8f6f4 v[126:129], v[26:33], v[58:65], 0, v246, v246 op_sel_hi:[0,0,0]
	v_mfma_scale_f32_16x16x128_f8f6f4 v[122:125], v[18:25], v[58:65], 0, v246, v246 op_sel_hi:[0,0,0]
	v_mfma_scale_f32_16x16x128_f8f6f4 v[110:113], v[26:33], v[50:57], 0, v246, v246 op_sel_hi:[0,0,0]
	v_mfma_scale_f32_16x16x128_f8f6f4 v[106:109], v[18:25], v[50:57], 0, v246, v246 op_sel_hi:[0,0,0]
	v_mfma_scale_f32_16x16x128_f8f6f4 v[94:97], v[26:33], v[42:49], 0, v246, v246 op_sel_hi:[0,0,0]
	v_mfma_scale_f32_16x16x128_f8f6f4 v[90:93], v[18:25], v[42:49], 0, v246, v246 op_sel_hi:[0,0,0]
	v_mfma_scale_f32_16x16x128_f8f6f4 v[78:81], v[26:33], v[34:41], 0, v246, v246 op_sel_hi:[0,0,0]
	v_mfma_scale_f32_16x16x128_f8f6f4 v[74:77], v[18:25], v[34:41], 0, v246, v246 op_sel_hi:[0,0,0]
	s_setprio 0
	s_setprio 1
	v_mfma_scale_f32_16x16x128_f8f6f4 v[118:121], v[10:17], v[58:65], 0, v246, v246 op_sel_hi:[0,0,0]
	v_mfma_scale_f32_16x16x128_f8f6f4 v[114:117], v[2:9], v[58:65], 0, v246, v246 op_sel_hi:[0,0,0]
	v_mfma_scale_f32_16x16x128_f8f6f4 v[102:105], v[10:17], v[50:57], 0, v246, v246 op_sel_hi:[0,0,0]
	v_mfma_scale_f32_16x16x128_f8f6f4 v[98:101], v[2:9], v[50:57], 0, v246, v246 op_sel_hi:[0,0,0]
	v_mfma_scale_f32_16x16x128_f8f6f4 v[86:89], v[10:17], v[42:49], 0, v246, v246 op_sel_hi:[0,0,0]
	v_mfma_scale_f32_16x16x128_f8f6f4 v[82:85], v[2:9], v[42:49], 0, v246, v246 op_sel_hi:[0,0,0]
	v_mfma_scale_f32_16x16x128_f8f6f4 v[70:73], v[10:17], v[34:41], 0, v246, v246 op_sel_hi:[0,0,0]
	v_mfma_scale_f32_16x16x128_f8f6f4 v[66:69], v[2:9], v[34:41], 0, v246, v246 op_sel_hi:[0,0,0]
	s_branch .Lpl1531_join

; #define PG8_STAGE(bufoff, gbase, voff) do { _Pragma("unroll") for (int _i = 0; _i < 2; ++_i) \
;         __builtin_amdgcn_global_load_lds((const unsigned*)((const char*)(gbase) + (voff)[_i]), (LAS unsigned*)(lds + (bufoff) + ldsw + _i * 8192), 16, 0, 0); } while (0)
; #define PG8_STAGEA(bufoff, h, ap, kb, go) do { if constexpr (GATHER) { PG8_STAGE(bufoff, (const char*)g.A + (kb), go[h]); } else { PG8_STAGE(bufoff, (ap) + (h) * hstep, voffA); } } while (0)
; #define PG8_WAIT_V(n) asm volatile("s_waitcnt vmcnt(" #n ")" ::: "memory")
; #define PG8_WAIT_L(n) asm volatile("s_waitcnt lgkmcnt(" #n ")" ::: "memory")
; #define PG8_BAR __builtin_amdgcn_s_barrier()
; #define PG8_SCHED __builtin_amdgcn_sched_barrier(0)
; template <class Epi, class Sched, bool GATHER, bool FP8 = false>
; __device__ __forceinline__ void gemm_phase(LAS unsigned char* lds, LAS int* idx, const Gemm g, const Sched& S, const Epi& E) {
;     ...
;             PG8_LDB(B0, 1, 0); PG8_LDB(B1, 1, 1); PG8_SCHED; PG8_LDA(At, 1, 0); PG8_STAGEA(PG8_SA(0, 1), 1, a2, k2, g2);
;             PG8_WAIT_V(8); PG8_WAIT_L(0); PG8_BAR; PG8_MMA(0, 0, At, B0); PG8_MMA(0, 1, At, B1); PG8_BAR; PG8_SCHED;
;             PG8_LDA(At, 1, 1); PG8_STAGE(PG8_SB(1, 0), b3, voffB); PG8_STAGE(PG8_SB(1, 1), b3 + hstepB, voffB); PG8_STAGEA(PG8_SA(1, 0), 0, a3, k3, g2);
;             PG8_WAIT_V(8); PG8_WAIT_L(0); PG8_BAR; PG8_MMA(1, 0, At, B0); PG8_MMA(1, 1, At, B1); PG8_BAR; PG8_SCHED;
;             if constexpr (GATHER) { if (last) { _Pragma("unroll") for (int h = 0; h < 2; ++h) _Pragma("unroll") for (int i = 0; i < 2; ++i) gc[h][i] = g2[h][i]; } }
.Lpl1531_join:
	s_setprio 0
	s_barrier
	ds_read_b128 v[2:5], v237
	ds_read_b128 v[6:9], v238
	ds_read_b128 v[10:13], v239
	ds_read_b128 v[14:17], v240
	ds_read_b128 v[18:21], v241
	ds_read_b128 v[22:25], v242
	ds_read_b128 v[26:29], v243
	ds_read_b128 v[30:33], v244
	s_mov_b32 m0, s59
	ds_read_b128 v[34:37], v247 offset:32768
	ds_read_b128 v[38:41], v247 offset:33792
	ds_read_b128 v[42:45], v247 offset:34816
	ds_read_b128 v[46:49], v247 offset:35840
	ds_read_b128 v[50:53], v247 offset:36864
	ds_read_b128 v[54:57], v247 offset:37888
	ds_read_b128 v[58:61], v247 offset:38912
	ds_read_b128 v[62:65], v247 offset:39936
	global_load_lds_dwordx4 v212, s[42:43]
	s_mov_b32 m0, s60
	s_nop 0
	global_load_lds_dwordx4 v214, s[42:43]
	s_waitcnt vmcnt(8)
	s_waitcnt lgkmcnt(0)
	s_barrier
	s_setprio 1
	s_waitcnt lgkmcnt(0)
	v_mfma_scale_f32_16x16x128_f8f6f4 v[190:193], v[2:9], v[34:41], v[190:193], v246, v246 op_sel_hi:[0,0,0]
	v_mfma_scale_f32_16x16x128_f8f6f4 v[186:189], v[10:17], v[34:41], v[186:189], v246, v246 op_sel_hi:[0,0,0]
	v_mfma_scale_f32_16x16x128_f8f6f4 v[174:177], v[2:9], v[42:49], v[174:177], v246, v246 op_sel_hi:[0,0,0]
	v_mfma_scale_f32_16x16x128_f8f6f4 v[170:173], v[10:17], v[42:49], v[170:173], v246, v246 op_sel_hi:[0,0,0]
	v_mfma_scale_f32_16x16x128_f8f6f4 v[158:161], v[2:9], v[50:57], v[158:161], v246, v246 op_sel_hi:[0,0,0]
	v_mfma_scale_f32_16x16x128_f8f6f4 v[154:157], v[10:17], v[50:57], v[154:157], v246, v246 op_sel_hi:[0,0,0]
	v_mfma_scale_f32_16x16x128_f8f6f4 v[142:145], v[2:9], v[58:65], v[142:145], v246, v246 op_sel_hi:[0,0,0]
	v_mfma_scale_f32_16x16x128_f8f6f4 v[138:141], v[10:17], v[58:65], v[138:141], v246, v246 op_sel_hi:[0,0,0]
	s_setprio 0
	s_setprio 1
	v_mfma_scale_f32_16x16x128_f8f6f4 v[182:185], v[18:25], v[34:41], v[182:185], v246, v246 op_sel_hi:[0,0,0]
	v_mfma_scale_f32_16x16x128_f8f6f4 v[178:181], v[26:33], v[34:41], v[178:181], v246, v246 op_sel_hi:[0,0,0]
	v_mfma_scale_f32_16x16x128_f8f6f4 v[166:169], v[18:25], v[42:49], v[166:169], v246, v246 op_sel_hi:[0,0,0]
	v_mfma_scale_f32_16x16x128_f8f6f4 v[162:165], v[26:33], v[42:49], v[162:165], v246, v246 op_sel_hi:[0,0,0]
	v_mfma_scale_f32_16x16x128_f8f6f4 v[150:153], v[18:25], v[50:57], v[150:153], v246, v246 op_sel_hi:[0,0,0]
	v_mfma_scale_f32_16x16x128_f8f6f4 v[146:149], v[26:33], v[50:57], v[146:149], v246, v246 op_sel_hi:[0,0,0]
	v_mfma_scale_f32_16x16x128_f8f6f4 v[134:137], v[18:25], v[58:65], v[134:137], v246, v246 op_sel_hi:[0,0,0]
	v_mfma_scale_f32_16x16x128_f8f6f4 v[130:133], v[26:33], v[58:65], v[130:133], v246, v246 op_sel_hi:[0,0,0]
	s_setprio 0
	s_barrier
	s_mov_b32 m0, s66
	v_lshl_add_u64 v[218:219], v[218:219], 0, s[12:13]
	ds_read_b128 v[34:37], v247 offset:49152
	ds_read_b128 v[38:41], v247 offset:50176
	ds_read_b128 v[42:45], v247 offset:51200
	ds_read_b128 v[46:49], v247 offset:52224
	ds_read_b128 v[50:53], v247 offset:53248
	ds_read_b128 v[54:57], v247 offset:54272
	ds_read_b128 v[58:61], v247 offset:55296
	ds_read_b128 v[62:65], v247 offset:56320
	global_load_lds_dwordx4 v[218:219], off
	v_lshl_add_u64 v[218:219], v[220:221], 0, s[12:13]
	s_mov_b32 m0, s67
	s_nop 0
	global_load_lds_dwordx4 v[218:219], off
	v_lshl_add_u64 v[218:219], v[222:223], 0, s[12:13]
	s_mov_b32 m0, s71
	s_nop 0
	global_load_lds_dwordx4 v[218:219], off
	v_lshl_add_u64 v[218:219], v[224:225], 0, s[12:13]
	s_mov_b32 m0, s72
	s_nop 0
	global_load_lds_dwordx4 v[218:219], off
	v_lshl_add_u64 v[218:219], v[226:227], 0, s[12:13]
	s_mov_b32 m0, s69
	s_nop 0
	global_load_lds_dwordx4 v[218:219], off
	v_lshl_add_u64 v[218:219], v[228:229], 0, s[12:13]
	s_mov_b32 m0, s70
	s_nop 0
	global_load_lds_dwordx4 v[218:219], off
	s_waitcnt vmcnt(8)
	s_waitcnt lgkmcnt(0)
	s_barrier
	s_setprio 1
	s_waitcnt lgkmcnt(0)
	v_mfma_scale_f32_16x16x128_f8f6f4 v[126:129], v[2:9], v[34:41], v[126:129], v246, v246 op_sel_hi:[0,0,0]
	v_mfma_scale_f32_16x16x128_f8f6f4 v[122:125], v[10:17], v[34:41], v[122:125], v246, v246 op_sel_hi:[0,0,0]
	v_mfma_scale_f32_16x16x128_f8f6f4 v[110:113], v[2:9], v[42:49], v[110:113], v246, v246 op_sel_hi:[0,0,0]
	v_mfma_scale_f32_16x16x128_f8f6f4 v[106:109], v[10:17], v[42:49], v[106:109], v246, v246 op_sel_hi:[0,0,0]
	v_mfma_scale_f32_16x16x128_f8f6f4 v[94:97], v[2:9], v[50:57], v[94:97], v246, v246 op_sel_hi:[0,0,0]
	v_mfma_scale_f32_16x16x128_f8f6f4 v[90:93], v[10:17], v[50:57], v[90:93], v246, v246 op_sel_hi:[0,0,0]
	v_mfma_scale_f32_16x16x128_f8f6f4 v[78:81], v[2:9], v[58:65], v[78:81], v246, v246 op_sel_hi:[0,0,0]
	v_mfma_scale_f32_16x16x128_f8f6f4 v[74:77], v[10:17], v[58:65], v[74:77], v246, v246 op_sel_hi:[0,0,0]
	s_setprio 0
	s_setprio 1
	v_mfma_scale_f32_16x16x128_f8f6f4 v[118:121], v[18:25], v[34:41], v[118:121], v246, v246 op_sel_hi:[0,0,0]
	v_mfma_scale_f32_16x16x128_f8f6f4 v[114:117], v[26:33], v[34:41], v[114:117], v246, v246 op_sel_hi:[0,0,0]
	v_mfma_scale_f32_16x16x128_f8f6f4 v[102:105], v[18:25], v[42:49], v[102:105], v246, v246 op_sel_hi:[0,0,0]
	v_mfma_scale_f32_16x16x128_f8f6f4 v[98:101], v[26:33], v[42:49], v[98:101], v246, v246 op_sel_hi:[0,0,0]
	v_mfma_scale_f32_16x16x128_f8f6f4 v[86:89], v[18:25], v[50:57], v[86:89], v246, v246 op_sel_hi:[0,0,0]
	v_mfma_scale_f32_16x16x128_f8f6f4 v[82:85], v[26:33], v[50:57], v[82:85], v246, v246 op_sel_hi:[0,0,0]
	v_mfma_scale_f32_16x16x128_f8f6f4 v[70:73], v[18:25], v[58:65], v[70:73], v246, v246 op_sel_hi:[0,0,0]
	v_mfma_scale_f32_16x16x128_f8f6f4 v[66:69], v[26:33], v[58:65], v[66:69], v246, v246 op_sel_hi:[0,0,0]
	s_setprio 0
	s_barrier
	s_andn2_b64 vcc, exec, s[38:39]
	s_cbranch_vccnz .LBB0_1549
	v_mov_b32_e32 v200, v208
	v_mov_b32_e32 v204, v216
	v_mov_b32_e32 v202, v212
	v_mov_b32_e32 v206, v214
